# E2 on f16 MFMA 16x16x32 (f32 accumulate): up-rows gathered by LDS-DMA into the per-wave ring, read transposed with ds_read_b64_tr_b4 (16 experts of one dim per lane), fp4->f16 exact; gate weights via
# speedup vs baseline: 1.0906x; 1.0146x over previous
.Le2w_first:
	s_mov_b64 exec, 1
	global_atomic_add v251, v211, v1, s[24:25] sc0
	s_mov_b64 exec, -1
	v_mov_b32_e32 v198, 0x80
	v_and_b32_e32 v233, 7, v0
	v_xor_b32_e32 v166, 0, v233
	v_lshlrev_b32_e32 v166, 4, v166
	v_xor_b32_e32 v167, 1, v233
	v_lshlrev_b32_e32 v167, 4, v167
	v_xor_b32_e32 v168, 2, v233
	v_lshlrev_b32_e32 v168, 4, v168
	v_xor_b32_e32 v169, 3, v233
	v_lshlrev_b32_e32 v169, 4, v169
	v_xor_b32_e32 v170, 4, v233
	v_lshlrev_b32_e32 v170, 4, v170
	v_xor_b32_e32 v171, 5, v233
	v_lshlrev_b32_e32 v171, 4, v171
	v_xor_b32_e32 v172, 6, v233
	v_lshlrev_b32_e32 v172, 4, v172
	v_xor_b32_e32 v173, 7, v233
	v_lshlrev_b32_e32 v173, 4, v173
	v_lshrrev_b32_e32 v234, 6, v0
	s_nop 0
	v_readfirstlane_b32 s38, v234
	s_lshl_b32 s38, s38, 14
	v_bfe_u32 v234, v0, 4, 2
	v_and_b32_e32 v196, 1, v234
	v_and_b32_e32 v197, 2, v234
	v_bfe_u32 v235, v0, 3, 1
	v_xor_b32_e32 v236, v235, v196
	v_lshl_add_u32 v236, v234, 1, v236
	v_lshl_add_u32 v236, v233, 3, v236
	v_lshlrev_b32_e32 v236, 7, v236
	v_lshl_add_u32 v236, v235, 3, v236
	v_add_u32_e32 v236, s38, v236
	v_xor_b32_e32 v237, 0, v233
	v_lshl_add_u32 v150, v237, 4, v236
	v_xor_b32_e32 v158, 8, v150
	v_xor_b32_e32 v237, 1, v233
	v_lshl_add_u32 v151, v237, 4, v236
	v_xor_b32_e32 v159, 8, v151
	v_xor_b32_e32 v237, 2, v233
	v_lshl_add_u32 v152, v237, 4, v236
	v_xor_b32_e32 v160, 8, v152
	v_xor_b32_e32 v237, 3, v233
	v_lshl_add_u32 v153, v237, 4, v236
	v_xor_b32_e32 v161, 8, v153
	v_xor_b32_e32 v237, 4, v233
	v_lshl_add_u32 v154, v237, 4, v236
	v_xor_b32_e32 v162, 8, v154
	v_xor_b32_e32 v237, 5, v233
	v_lshl_add_u32 v155, v237, 4, v236
	v_xor_b32_e32 v163, 8, v155
	v_xor_b32_e32 v237, 6, v233
	v_lshl_add_u32 v156, v237, 4, v236
	v_xor_b32_e32 v164, 8, v156
	v_xor_b32_e32 v237, 7, v233
	v_lshl_add_u32 v157, v237, 4, v236
	v_xor_b32_e32 v165, 8, v157
	s_lshr_b32 s99, s38, 4
	s_add_i32 s99, s99, 0x21000
	v_lshl_add_u32 v237, v196, 5, s99
	v_lshl_add_u32 v174, v234, 6, v237
	v_xor_b32_e32 v175, 32, v174
	v_and_b32_e32 v237, 63, v0
	v_add_u32_e32 v237, s58, v237
	v_lshlrev_b32_e32 v184, 2, v237
	v_mov_b32_e32 v185, 0
	s_add_u32 s0, s56, 0xfffffef0
	s_addc_u32 s1, s57, -1
	s_lshl_b32 s42, s60, 3
	s_waitcnt vmcnt(0)
	v_readfirstlane_b32 s35, v251
	s_cmp_ge_i32 s35, s42
	s_cbranch_scc1 .LBB0_878
	s_lshr_b32 s99, s35, 3
	s_lshl_b32 s98, s99, 6
	s_and_b32 s99, s99, 0xffffff00
	s_add_i32 s99, s99, 0x100
	s_and_b64 s[2:3], s[30:31], exec
	s_cselect_b32 s99, 0, s99
	s_add_i32 s98, s98, s99
	s_and_b32 s99, s35, 7
	s_lshl_b32 s99, s99, 3
	s_add_i32 s98, s98, s99
	s_mov_b32 s39, s98
	v_bfe_u32 v234, v0, 3, 3
	s_lshl_b32 s99, s98, 8
	v_lshl_add_u32 v176, v234, 5, s99
	v_and_b32_e32 v235, 15, v0
	v_lshl_add_u32 v177, v235, 4, s99
	global_load_dwordx4 v[98:101], v176, s[22:23]
	global_load_dwordx4 v[102:105], v176, s[22:23] offset:16
	v_add_u32_e32 v176, 0x100, v176
	global_load_dwordx4 v[106:109], v176, s[22:23]
	global_load_dwordx4 v[110:113], v176, s[22:23] offset:16
	v_add_u32_e32 v176, 0x100, v176
	s_lshr_b32 s99, s38, 4
	s_add_i32 m0, s99, 0x21000
	s_mov_b64 exec, 0xffff
	global_load_lds_dwordx4 v177, s[0:1]
	s_mov_b64 exec, -1
	v_add_u32_e32 v177, 0x100, v177
	s_waitcnt vmcnt(3)
	s_add_i32 m0, s38, 0x0
	v_mad_u32_u16 v178, v98, v198, v166
	global_load_lds_dwordx4 v178, s[40:41]
	s_add_i32 m0, s38, 0x400
	v_mad_u32_u16 v179, v98, v198, v167 op_sel:[1,0,0,0]
	global_load_lds_dwordx4 v179, s[40:41]
	s_add_i32 m0, s38, 0x800
	v_mad_u32_u16 v178, v99, v198, v168
	global_load_lds_dwordx4 v178, s[40:41]
	s_add_i32 m0, s38, 0xc00
	v_mad_u32_u16 v179, v99, v198, v169 op_sel:[1,0,0,0]
	global_load_lds_dwordx4 v179, s[40:41]
	s_add_i32 m0, s38, 0x1000
	v_mad_u32_u16 v178, v100, v198, v170
	global_load_lds_dwordx4 v178, s[40:41]
	s_add_i32 m0, s38, 0x1400
	v_mad_u32_u16 v179, v100, v198, v171 op_sel:[1,0,0,0]
	global_load_lds_dwordx4 v179, s[40:41]
	s_add_i32 m0, s38, 0x1800
	v_mad_u32_u16 v178, v101, v198, v172
	global_load_lds_dwordx4 v178, s[40:41]
	s_add_i32 m0, s38, 0x1c00
	v_mad_u32_u16 v179, v101, v198, v173 op_sel:[1,0,0,0]
	global_load_lds_dwordx4 v179, s[40:41]
	s_add_i32 m0, s38, 0x2000
	v_mad_u32_u16 v178, v102, v198, v166
	global_load_lds_dwordx4 v178, s[40:41]
	s_add_i32 m0, s38, 0x2400
	v_mad_u32_u16 v179, v102, v198, v167 op_sel:[1,0,0,0]
	global_load_lds_dwordx4 v179, s[40:41]
	s_add_i32 m0, s38, 0x2800
	v_mad_u32_u16 v178, v103, v198, v168
	global_load_lds_dwordx4 v178, s[40:41]
	s_add_i32 m0, s38, 0x2c00
	v_mad_u32_u16 v179, v103, v198, v169 op_sel:[1,0,0,0]
	global_load_lds_dwordx4 v179, s[40:41]
	s_add_i32 m0, s38, 0x3000
	v_mad_u32_u16 v178, v104, v198, v170
	global_load_lds_dwordx4 v178, s[40:41]
	s_add_i32 m0, s38, 0x3400
	v_mad_u32_u16 v179, v104, v198, v171 op_sel:[1,0,0,0]
	global_load_lds_dwordx4 v179, s[40:41]
	s_add_i32 m0, s38, 0x3800
	v_mad_u32_u16 v178, v105, v198, v172
	global_load_lds_dwordx4 v178, s[40:41]
	s_add_i32 m0, s38, 0x3c00
	v_mad_u32_u16 v179, v105, v198, v173 op_sel:[1,0,0,0]
	global_load_lds_dwordx4 v179, s[40:41]
	v_mov_b32_e32 v194, s98
	v_mul_hi_i32 v186, v194, s69
	v_lshrrev_b32_e32 v187, 31, v186
	v_ashrrev_i32_e32 v186, 13, v186
	v_add_u32_e32 v187, v186, v187
	v_mul_i32_i24_e32 v190, 0xffffbf00, v187
	v_add_u32_e32 v186, v194, v190
	v_cmp_gt_i32_e32 vcc, s68, v186
	v_cmp_lt_i32_e64 s[2:3], s21, v186
	s_and_saveexec_b64 s[98:99], s[2:3]
	s_xor_b64 s[2:3], exec, s[98:99]
	v_lshl_add_u32 v186, v187, 14, v190
	v_add3_u32 v186, v194, v186, s88
	s_or_saveexec_b64 s[2:3], s[2:3]
	v_mov_b64_e32 v[188:189], s[18:19]
	s_xor_b64 exec, exec, s[2:3]
	v_lshlrev_b32_e32 v186, 8, v187
	v_add3_u32 v186, v190, v194, v186
	v_mov_b64_e32 v[188:189], s[72:73]
	s_or_b64 exec, exec, s[2:3]
	v_mul_i32_i24_e32 v187, 0x3000, v187
	v_cndmask_b32_e32 v190, v187, v223, vcc
	v_ashrrev_i32_e32 v191, 31, v190
	v_lshl_add_u64 v[190:191], v[190:191], 2, s[10:11]
	v_ashrrev_i32_e32 v187, 31, v186
	v_lshl_add_u64 v[192:193], v[190:191], 0, v[184:185]
	v_lshlrev_b64 v[186:187], 13, v[186:187]
	v_lshl_add_u64 v[186:187], v[188:189], 0, v[186:187]
	v_add_co_u32_e32 v192, vcc, s94, v192
	v_lshl_add_u64 v[180:181], v[186:187], 0, v[184:185]
	s_nop 0
	v_addc_co_u32_e32 v193, vcc, 0, v193, vcc
	global_load_dword v134, v[192:193], off
	global_load_dword v135, v[192:193], off offset:256
	global_load_dword v136, v[192:193], off offset:512
	global_load_dword v137, v[192:193], off offset:768
	s_mov_b32 s33, 0
	s_mov_b32 s43, 0
	s_waitcnt vmcnt(0)
	ds_read_b64_tr_b4 v[114:115], v150
	ds_read_b64_tr_b4 v[116:117], v158
	ds_read_b128 v[66:69], v174
	ds_read_b128 v[70:73], v174 offset:16
	ds_read_b128 v[74:77], v175
	ds_read_b128 v[78:81], v175 offset:16
.Le2_loop:
	s_cmp_eq_u32 s33, 2
	s_cbranch_scc0 .Le2_noatom
	s_mov_b64 exec, 1
	global_atomic_add v251, v211, v1, s[24:25] sc0
	s_mov_b64 exec, -1
.Le2_noatom:
	s_cmp_eq_u32 s33, 4
	s_cbranch_scc0 .Le2_noprep
	v_readfirstlane_b32 s35, v251
	s_mov_b32 s43, -7
	s_cmp_ge_i32 s35, s42
	s_cbranch_scc1 .Le2_nonext
	s_lshr_b32 s99, s35, 3
	s_lshl_b32 s98, s99, 6
	s_and_b32 s99, s99, 0xffffff00
	s_add_i32 s99, s99, 0x100
	s_and_b64 s[2:3], s[30:31], exec
	s_cselect_b32 s99, 0, s99
	s_add_i32 s98, s98, s99
	s_and_b32 s99, s35, 7
	s_lshl_b32 s99, s99, 3
	s_add_i32 s98, s98, s99
	s_sub_i32 s43, s98, s39
	s_add_i32 s43, s43, -7
	v_mov_b32_e32 v194, s98
	v_mul_hi_i32 v186, v194, s69
	v_lshrrev_b32_e32 v187, 31, v186
	v_ashrrev_i32_e32 v186, 13, v186
	v_add_u32_e32 v187, v186, v187
	v_mul_i32_i24_e32 v190, 0xffffbf00, v187
	v_add_u32_e32 v186, v194, v190
	v_cmp_gt_i32_e32 vcc, s68, v186
	v_cmp_lt_i32_e64 s[2:3], s21, v186
	s_and_saveexec_b64 s[98:99], s[2:3]
	s_xor_b64 s[2:3], exec, s[98:99]
	v_lshl_add_u32 v186, v187, 14, v190
	v_add3_u32 v186, v194, v186, s88
	s_or_saveexec_b64 s[2:3], s[2:3]
	v_mov_b64_e32 v[188:189], s[18:19]
	s_xor_b64 exec, exec, s[2:3]
	v_lshlrev_b32_e32 v186, 8, v187
	v_add3_u32 v186, v190, v194, v186
	v_mov_b64_e32 v[188:189], s[72:73]
	s_or_b64 exec, exec, s[2:3]
	v_mul_i32_i24_e32 v187, 0x3000, v187
	v_cndmask_b32_e32 v190, v187, v223, vcc
	v_ashrrev_i32_e32 v191, 31, v190
	v_lshl_add_u64 v[190:191], v[190:191], 2, s[10:11]
	v_ashrrev_i32_e32 v187, 31, v186
	v_lshl_add_u64 v[192:193], v[190:191], 0, v[184:185]
	v_lshlrev_b64 v[186:187], 13, v[186:187]
	v_lshl_add_u64 v[186:187], v[188:189], 0, v[186:187]
	v_add_co_u32_e32 v192, vcc, s94, v192
	v_lshl_add_u64 v[182:183], v[186:187], 0, v[184:185]
	s_nop 0
	v_addc_co_u32_e32 v193, vcc, 0, v193, vcc
	global_load_dword v138, v[192:193], off
	global_load_dword v139, v[192:193], off offset:256
	global_load_dword v140, v[192:193], off offset:512
	global_load_dword v141, v[192:193], off offset:768
	s_branch .Le2_noprep

.Le2_noprep:
	s_lshr_b32 s99, s38, 4
	s_add_i32 m0, s99, 0x21100
	s_mov_b64 exec, 0xffff
	global_load_lds_dwordx4 v177, s[0:1]
	s_mov_b64 exec, -1
	s_lshl_b32 s99, s43, 8
	s_cmp_eq_u32 s33, 6
	s_cselect_b32 s99, s99, 0x100
	v_add_u32_e32 v177, s99, v177
	global_load_dwordx4 v[98:101], v176, s[22:23]
	global_load_dwordx4 v[102:105], v176, s[22:23] offset:16
	v_add_u32_e32 v176, 0x100, v176
	global_load_dword v130, v[180:181], off
	global_load_dword v131, v[180:181], off offset:256
	global_load_dword v132, v[180:181], off offset:512
	global_load_dword v133, v[180:181], off offset:768
	ds_read_b64_tr_b4 v[118:119], v151
	ds_read_b64_tr_b4 v[120:121], v159
	s_waitcnt lgkmcnt(2)
	v_cvt_scalef32_pk_f16_fp4 v122, v114, 1.0
	v_cvt_scalef32_pk_f16_fp4 v123, v114, 1.0 op_sel:[1,0,0]
	v_cvt_scalef32_pk_f16_fp4 v124, v114, 1.0 op_sel:[0,1,0]
	v_cvt_scalef32_pk_f16_fp4 v125, v114, 1.0 op_sel:[1,1,0]
	v_cvt_scalef32_pk_f16_fp4 v126, v116, 1.0
	v_cvt_scalef32_pk_f16_fp4 v127, v116, 1.0 op_sel:[1,0,0]
	v_cvt_scalef32_pk_f16_fp4 v128, v116, 1.0 op_sel:[0,1,0]
	v_cvt_scalef32_pk_f16_fp4 v129, v116, 1.0 op_sel:[1,1,0]
	v_mfma_f32_16x16x32_f16 v[2:5], v[66:69], v[122:125], 0
	v_cvt_scalef32_pk_f16_fp4 v122, v117, 1.0
	v_cvt_scalef32_pk_f16_fp4 v123, v117, 1.0 op_sel:[1,0,0]
	v_cvt_scalef32_pk_f16_fp4 v124, v117, 1.0 op_sel:[0,1,0]
	v_cvt_scalef32_pk_f16_fp4 v125, v117, 1.0 op_sel:[1,1,0]
	v_mfma_f32_16x16x32_f16 v[6:9], v[66:69], v[126:129], 0
	v_cvt_scalef32_pk_f16_fp4 v126, v115, 1.0
	v_cvt_scalef32_pk_f16_fp4 v127, v115, 1.0 op_sel:[1,0,0]
	v_cvt_scalef32_pk_f16_fp4 v128, v115, 1.0 op_sel:[0,1,0]
	v_cvt_scalef32_pk_f16_fp4 v129, v115, 1.0 op_sel:[1,1,0]
	v_mfma_f32_16x16x32_f16 v[2:5], v[74:77], v[122:125], v[2:5]
	v_mfma_f32_16x16x32_f16 v[6:9], v[74:77], v[126:129], v[6:9]
	ds_read_b64_tr_b4 v[114:115], v152
	ds_read_b64_tr_b4 v[116:117], v160
	s_waitcnt lgkmcnt(2)
	v_cvt_scalef32_pk_f16_fp4 v122, v118, 1.0
	v_cvt_scalef32_pk_f16_fp4 v123, v118, 1.0 op_sel:[1,0,0]
	v_cvt_scalef32_pk_f16_fp4 v124, v118, 1.0 op_sel:[0,1,0]
	v_cvt_scalef32_pk_f16_fp4 v125, v118, 1.0 op_sel:[1,1,0]
	v_cvt_scalef32_pk_f16_fp4 v126, v120, 1.0
	v_cvt_scalef32_pk_f16_fp4 v127, v120, 1.0 op_sel:[1,0,0]
	v_cvt_scalef32_pk_f16_fp4 v128, v120, 1.0 op_sel:[0,1,0]
	v_cvt_scalef32_pk_f16_fp4 v129, v120, 1.0 op_sel:[1,1,0]
	v_mfma_f32_16x16x32_f16 v[10:13], v[66:69], v[122:125], 0
	v_cvt_scalef32_pk_f16_fp4 v122, v121, 1.0
	v_cvt_scalef32_pk_f16_fp4 v123, v121, 1.0 op_sel:[1,0,0]
	v_cvt_scalef32_pk_f16_fp4 v124, v121, 1.0 op_sel:[0,1,0]
	v_cvt_scalef32_pk_f16_fp4 v125, v121, 1.0 op_sel:[1,1,0]
	v_mfma_f32_16x16x32_f16 v[14:17], v[66:69], v[126:129], 0
	v_cvt_scalef32_pk_f16_fp4 v126, v119, 1.0
	v_cvt_scalef32_pk_f16_fp4 v127, v119, 1.0 op_sel:[1,0,0]
	v_cvt_scalef32_pk_f16_fp4 v128, v119, 1.0 op_sel:[0,1,0]
	v_cvt_scalef32_pk_f16_fp4 v129, v119, 1.0 op_sel:[1,1,0]
	v_mfma_f32_16x16x32_f16 v[10:13], v[74:77], v[122:125], v[10:13]
	v_mfma_f32_16x16x32_f16 v[14:17], v[74:77], v[126:129], v[14:17]
	ds_read_b64_tr_b4 v[118:119], v153
	ds_read_b64_tr_b4 v[120:121], v161
	s_waitcnt lgkmcnt(2)
	v_cvt_scalef32_pk_f16_fp4 v122, v114, 1.0
	v_cvt_scalef32_pk_f16_fp4 v123, v114, 1.0 op_sel:[1,0,0]
	v_cvt_scalef32_pk_f16_fp4 v124, v114, 1.0 op_sel:[0,1,0]
	v_cvt_scalef32_pk_f16_fp4 v125, v114, 1.0 op_sel:[1,1,0]
	v_cvt_scalef32_pk_f16_fp4 v126, v116, 1.0
	v_cvt_scalef32_pk_f16_fp4 v127, v116, 1.0 op_sel:[1,0,0]
	v_cvt_scalef32_pk_f16_fp4 v128, v116, 1.0 op_sel:[0,1,0]
	v_cvt_scalef32_pk_f16_fp4 v129, v116, 1.0 op_sel:[1,1,0]
	v_mfma_f32_16x16x32_f16 v[18:21], v[66:69], v[122:125], 0
	v_cvt_scalef32_pk_f16_fp4 v122, v117, 1.0
	v_cvt_scalef32_pk_f16_fp4 v123, v117, 1.0 op_sel:[1,0,0]
	v_cvt_scalef32_pk_f16_fp4 v124, v117, 1.0 op_sel:[0,1,0]
	v_cvt_scalef32_pk_f16_fp4 v125, v117, 1.0 op_sel:[1,1,0]
	v_mfma_f32_16x16x32_f16 v[22:25], v[66:69], v[126:129], 0
	v_cvt_scalef32_pk_f16_fp4 v126, v115, 1.0
	v_cvt_scalef32_pk_f16_fp4 v127, v115, 1.0 op_sel:[1,0,0]
	v_cvt_scalef32_pk_f16_fp4 v128, v115, 1.0 op_sel:[0,1,0]
	v_cvt_scalef32_pk_f16_fp4 v129, v115, 1.0 op_sel:[1,1,0]
	v_mfma_f32_16x16x32_f16 v[18:21], v[74:77], v[122:125], v[18:21]
	v_mfma_f32_16x16x32_f16 v[22:25], v[74:77], v[126:129], v[22:25]
	ds_read_b64_tr_b4 v[114:115], v154
	ds_read_b64_tr_b4 v[116:117], v162
	s_waitcnt lgkmcnt(2)
	v_cvt_scalef32_pk_f16_fp4 v122, v118, 1.0
	v_cvt_scalef32_pk_f16_fp4 v123, v118, 1.0 op_sel:[1,0,0]
	v_cvt_scalef32_pk_f16_fp4 v124, v118, 1.0 op_sel:[0,1,0]
	v_cvt_scalef32_pk_f16_fp4 v125, v118, 1.0 op_sel:[1,1,0]
	v_cvt_scalef32_pk_f16_fp4 v126, v120, 1.0
	v_cvt_scalef32_pk_f16_fp4 v127, v120, 1.0 op_sel:[1,0,0]
	v_cvt_scalef32_pk_f16_fp4 v128, v120, 1.0 op_sel:[0,1,0]
	v_cvt_scalef32_pk_f16_fp4 v129, v120, 1.0 op_sel:[1,1,0]
	v_mfma_f32_16x16x32_f16 v[26:29], v[66:69], v[122:125], 0
	v_cvt_scalef32_pk_f16_fp4 v122, v121, 1.0
	v_cvt_scalef32_pk_f16_fp4 v123, v121, 1.0 op_sel:[1,0,0]
	v_cvt_scalef32_pk_f16_fp4 v124, v121, 1.0 op_sel:[0,1,0]
	v_cvt_scalef32_pk_f16_fp4 v125, v121, 1.0 op_sel:[1,1,0]
	v_mfma_f32_16x16x32_f16 v[30:33], v[66:69], v[126:129], 0
	v_cvt_scalef32_pk_f16_fp4 v126, v119, 1.0
	v_cvt_scalef32_pk_f16_fp4 v127, v119, 1.0 op_sel:[1,0,0]
	v_cvt_scalef32_pk_f16_fp4 v128, v119, 1.0 op_sel:[0,1,0]
	v_cvt_scalef32_pk_f16_fp4 v129, v119, 1.0 op_sel:[1,1,0]
	v_mfma_f32_16x16x32_f16 v[26:29], v[74:77], v[122:125], v[26:29]
	v_mfma_f32_16x16x32_f16 v[30:33], v[74:77], v[126:129], v[30:33]
	ds_read_b64_tr_b4 v[118:119], v155
	ds_read_b64_tr_b4 v[120:121], v163
	s_waitcnt lgkmcnt(2)
	v_cvt_scalef32_pk_f16_fp4 v122, v114, 1.0
	v_cvt_scalef32_pk_f16_fp4 v123, v114, 1.0 op_sel:[1,0,0]
	v_cvt_scalef32_pk_f16_fp4 v124, v114, 1.0 op_sel:[0,1,0]
	v_cvt_scalef32_pk_f16_fp4 v125, v114, 1.0 op_sel:[1,1,0]
	v_cvt_scalef32_pk_f16_fp4 v126, v116, 1.0
	v_cvt_scalef32_pk_f16_fp4 v127, v116, 1.0 op_sel:[1,0,0]
	v_cvt_scalef32_pk_f16_fp4 v128, v116, 1.0 op_sel:[0,1,0]
	v_cvt_scalef32_pk_f16_fp4 v129, v116, 1.0 op_sel:[1,1,0]
	v_mfma_f32_16x16x32_f16 v[34:37], v[66:69], v[122:125], 0
	v_cvt_scalef32_pk_f16_fp4 v122, v117, 1.0
	v_cvt_scalef32_pk_f16_fp4 v123, v117, 1.0 op_sel:[1,0,0]
	v_cvt_scalef32_pk_f16_fp4 v124, v117, 1.0 op_sel:[0,1,0]
	v_cvt_scalef32_pk_f16_fp4 v125, v117, 1.0 op_sel:[1,1,0]
	v_mfma_f32_16x16x32_f16 v[38:41], v[66:69], v[126:129], 0
	v_cvt_scalef32_pk_f16_fp4 v126, v115, 1.0
	v_cvt_scalef32_pk_f16_fp4 v127, v115, 1.0 op_sel:[1,0,0]
	v_cvt_scalef32_pk_f16_fp4 v128, v115, 1.0 op_sel:[0,1,0]
	v_cvt_scalef32_pk_f16_fp4 v129, v115, 1.0 op_sel:[1,1,0]
	v_mfma_f32_16x16x32_f16 v[34:37], v[74:77], v[122:125], v[34:37]
	v_mfma_f32_16x16x32_f16 v[38:41], v[74:77], v[126:129], v[38:41]
	ds_read_b64_tr_b4 v[114:115], v156
	ds_read_b64_tr_b4 v[116:117], v164
	s_waitcnt lgkmcnt(2)
	v_cvt_scalef32_pk_f16_fp4 v122, v118, 1.0
	v_cvt_scalef32_pk_f16_fp4 v123, v118, 1.0 op_sel:[1,0,0]
	v_cvt_scalef32_pk_f16_fp4 v124, v118, 1.0 op_sel:[0,1,0]
	v_cvt_scalef32_pk_f16_fp4 v125, v118, 1.0 op_sel:[1,1,0]
	v_cvt_scalef32_pk_f16_fp4 v126, v120, 1.0
	v_cvt_scalef32_pk_f16_fp4 v127, v120, 1.0 op_sel:[1,0,0]
	v_cvt_scalef32_pk_f16_fp4 v128, v120, 1.0 op_sel:[0,1,0]
	v_cvt_scalef32_pk_f16_fp4 v129, v120, 1.0 op_sel:[1,1,0]
	v_mfma_f32_16x16x32_f16 v[42:45], v[66:69], v[122:125], 0
	v_cvt_scalef32_pk_f16_fp4 v122, v121, 1.0
	v_cvt_scalef32_pk_f16_fp4 v123, v121, 1.0 op_sel:[1,0,0]
	v_cvt_scalef32_pk_f16_fp4 v124, v121, 1.0 op_sel:[0,1,0]
	v_cvt_scalef32_pk_f16_fp4 v125, v121, 1.0 op_sel:[1,1,0]
	v_mfma_f32_16x16x32_f16 v[46:49], v[66:69], v[126:129], 0
	v_cvt_scalef32_pk_f16_fp4 v126, v119, 1.0
	v_cvt_scalef32_pk_f16_fp4 v127, v119, 1.0 op_sel:[1,0,0]
	v_cvt_scalef32_pk_f16_fp4 v128, v119, 1.0 op_sel:[0,1,0]
	v_cvt_scalef32_pk_f16_fp4 v129, v119, 1.0 op_sel:[1,1,0]
	v_mfma_f32_16x16x32_f16 v[42:45], v[74:77], v[122:125], v[42:45]
	v_mfma_f32_16x16x32_f16 v[46:49], v[74:77], v[126:129], v[46:49]
	ds_read_b64_tr_b4 v[118:119], v157
	ds_read_b64_tr_b4 v[120:121], v165
	s_waitcnt lgkmcnt(2)
	v_cvt_scalef32_pk_f16_fp4 v122, v114, 1.0
	v_cvt_scalef32_pk_f16_fp4 v123, v114, 1.0 op_sel:[1,0,0]
	v_cvt_scalef32_pk_f16_fp4 v124, v114, 1.0 op_sel:[0,1,0]
	v_cvt_scalef32_pk_f16_fp4 v125, v114, 1.0 op_sel:[1,1,0]
	v_cvt_scalef32_pk_f16_fp4 v126, v116, 1.0
	v_cvt_scalef32_pk_f16_fp4 v127, v116, 1.0 op_sel:[1,0,0]
	v_cvt_scalef32_pk_f16_fp4 v128, v116, 1.0 op_sel:[0,1,0]
	v_cvt_scalef32_pk_f16_fp4 v129, v116, 1.0 op_sel:[1,1,0]
	v_mfma_f32_16x16x32_f16 v[50:53], v[66:69], v[122:125], 0
	v_cvt_scalef32_pk_f16_fp4 v122, v117, 1.0
	v_cvt_scalef32_pk_f16_fp4 v123, v117, 1.0 op_sel:[1,0,0]
	v_cvt_scalef32_pk_f16_fp4 v124, v117, 1.0 op_sel:[0,1,0]
	v_cvt_scalef32_pk_f16_fp4 v125, v117, 1.0 op_sel:[1,1,0]
	v_mfma_f32_16x16x32_f16 v[54:57], v[66:69], v[126:129], 0
	v_cvt_scalef32_pk_f16_fp4 v126, v115, 1.0
	v_cvt_scalef32_pk_f16_fp4 v127, v115, 1.0 op_sel:[1,0,0]
	v_cvt_scalef32_pk_f16_fp4 v128, v115, 1.0 op_sel:[0,1,0]
	v_cvt_scalef32_pk_f16_fp4 v129, v115, 1.0 op_sel:[1,1,0]
	v_mfma_f32_16x16x32_f16 v[50:53], v[74:77], v[122:125], v[50:53]
	v_mfma_f32_16x16x32_f16 v[54:57], v[74:77], v[126:129], v[54:57]
	s_waitcnt vmcnt(11)
	ds_read_b64_tr_b4 v[114:115], v150 offset:8192
	ds_read_b64_tr_b4 v[116:117], v158 offset:8192
	s_waitcnt lgkmcnt(2)
	s_add_i32 m0, s38, 0x0
	v_mad_u32_u16 v178, v106, v198, v166
	global_load_lds_dwordx4 v178, s[40:41]
	s_add_i32 m0, s38, 0x400
	v_mad_u32_u16 v179, v106, v198, v167 op_sel:[1,0,0,0]
	global_load_lds_dwordx4 v179, s[40:41]
	s_add_i32 m0, s38, 0x800
	v_mad_u32_u16 v178, v107, v198, v168
	global_load_lds_dwordx4 v178, s[40:41]
	s_add_i32 m0, s38, 0xc00
	v_mad_u32_u16 v179, v107, v198, v169 op_sel:[1,0,0,0]
	global_load_lds_dwordx4 v179, s[40:41]
	s_add_i32 m0, s38, 0x1000
	v_mad_u32_u16 v178, v108, v198, v170
	global_load_lds_dwordx4 v178, s[40:41]
	s_add_i32 m0, s38, 0x1400
	v_mad_u32_u16 v179, v108, v198, v171 op_sel:[1,0,0,0]
	global_load_lds_dwordx4 v179, s[40:41]
	s_add_i32 m0, s38, 0x1800
	v_mad_u32_u16 v178, v109, v198, v172
	global_load_lds_dwordx4 v178, s[40:41]
	s_add_i32 m0, s38, 0x1c00
	v_mad_u32_u16 v179, v109, v198, v173 op_sel:[1,0,0,0]
	global_load_lds_dwordx4 v179, s[40:41]
	v_cvt_scalef32_pk_f16_fp4 v122, v118, 1.0
	v_cvt_scalef32_pk_f16_fp4 v123, v118, 1.0 op_sel:[1,0,0]
	v_cvt_scalef32_pk_f16_fp4 v124, v118, 1.0 op_sel:[0,1,0]
	v_cvt_scalef32_pk_f16_fp4 v125, v118, 1.0 op_sel:[1,1,0]
	v_cvt_scalef32_pk_f16_fp4 v126, v120, 1.0
	v_cvt_scalef32_pk_f16_fp4 v127, v120, 1.0 op_sel:[1,0,0]
	v_cvt_scalef32_pk_f16_fp4 v128, v120, 1.0 op_sel:[0,1,0]
	v_cvt_scalef32_pk_f16_fp4 v129, v120, 1.0 op_sel:[1,1,0]
	v_mfma_f32_16x16x32_f16 v[58:61], v[66:69], v[122:125], 0
	v_cvt_scalef32_pk_f16_fp4 v122, v121, 1.0
	v_cvt_scalef32_pk_f16_fp4 v123, v121, 1.0 op_sel:[1,0,0]
	v_cvt_scalef32_pk_f16_fp4 v124, v121, 1.0 op_sel:[0,1,0]
	v_cvt_scalef32_pk_f16_fp4 v125, v121, 1.0 op_sel:[1,1,0]
	v_mfma_f32_16x16x32_f16 v[62:65], v[66:69], v[126:129], 0
	v_cvt_scalef32_pk_f16_fp4 v126, v119, 1.0
	v_cvt_scalef32_pk_f16_fp4 v127, v119, 1.0 op_sel:[1,0,0]
	v_cvt_scalef32_pk_f16_fp4 v128, v119, 1.0 op_sel:[0,1,0]
	v_cvt_scalef32_pk_f16_fp4 v129, v119, 1.0 op_sel:[1,1,0]
	v_mfma_f32_16x16x32_f16 v[58:61], v[74:77], v[122:125], v[58:61]
	v_mfma_f32_16x16x32_f16 v[62:65], v[74:77], v[126:129], v[62:65]
	ds_read_b64_tr_b4 v[118:119], v151 offset:8192
	ds_read_b64_tr_b4 v[120:121], v159 offset:8192
	s_waitcnt lgkmcnt(2)
	v_cvt_scalef32_pk_f16_fp4 v122, v114, 1.0
	v_cvt_scalef32_pk_f16_fp4 v123, v114, 1.0 op_sel:[1,0,0]
	v_cvt_scalef32_pk_f16_fp4 v124, v114, 1.0 op_sel:[0,1,0]
	v_cvt_scalef32_pk_f16_fp4 v125, v114, 1.0 op_sel:[1,1,0]
	v_cvt_scalef32_pk_f16_fp4 v126, v116, 1.0
	v_cvt_scalef32_pk_f16_fp4 v127, v116, 1.0 op_sel:[1,0,0]
	v_cvt_scalef32_pk_f16_fp4 v128, v116, 1.0 op_sel:[0,1,0]
	v_cvt_scalef32_pk_f16_fp4 v129, v116, 1.0 op_sel:[1,1,0]
	v_mfma_f32_16x16x32_f16 v[2:5], v[70:73], v[122:125], v[2:5]
	v_cvt_scalef32_pk_f16_fp4 v122, v117, 1.0
	v_cvt_scalef32_pk_f16_fp4 v123, v117, 1.0 op_sel:[1,0,0]
	v_cvt_scalef32_pk_f16_fp4 v124, v117, 1.0 op_sel:[0,1,0]
	v_cvt_scalef32_pk_f16_fp4 v125, v117, 1.0 op_sel:[1,1,0]
	v_mfma_f32_16x16x32_f16 v[6:9], v[70:73], v[126:129], v[6:9]
	v_cvt_scalef32_pk_f16_fp4 v126, v115, 1.0
	v_cvt_scalef32_pk_f16_fp4 v127, v115, 1.0 op_sel:[1,0,0]
	v_cvt_scalef32_pk_f16_fp4 v128, v115, 1.0 op_sel:[0,1,0]
	v_cvt_scalef32_pk_f16_fp4 v129, v115, 1.0 op_sel:[1,1,0]
	v_mfma_f32_16x16x32_f16 v[2:5], v[78:81], v[122:125], v[2:5]
	v_mfma_f32_16x16x32_f16 v[6:9], v[78:81], v[126:129], v[6:9]
	ds_read_b64_tr_b4 v[114:115], v152 offset:8192
	ds_read_b64_tr_b4 v[116:117], v160 offset:8192
	s_waitcnt lgkmcnt(2)
	v_cvt_scalef32_pk_f16_fp4 v122, v118, 1.0
	v_cvt_scalef32_pk_f16_fp4 v123, v118, 1.0 op_sel:[1,0,0]
	v_cvt_scalef32_pk_f16_fp4 v124, v118, 1.0 op_sel:[0,1,0]
	v_cvt_scalef32_pk_f16_fp4 v125, v118, 1.0 op_sel:[1,1,0]
	v_cvt_scalef32_pk_f16_fp4 v126, v120, 1.0
	v_cvt_scalef32_pk_f16_fp4 v127, v120, 1.0 op_sel:[1,0,0]
	v_cvt_scalef32_pk_f16_fp4 v128, v120, 1.0 op_sel:[0,1,0]
	v_cvt_scalef32_pk_f16_fp4 v129, v120, 1.0 op_sel:[1,1,0]
	v_mfma_f32_16x16x32_f16 v[10:13], v[70:73], v[122:125], v[10:13]
	v_cvt_scalef32_pk_f16_fp4 v122, v121, 1.0
	v_cvt_scalef32_pk_f16_fp4 v123, v121, 1.0 op_sel:[1,0,0]
	v_cvt_scalef32_pk_f16_fp4 v124, v121, 1.0 op_sel:[0,1,0]
	v_cvt_scalef32_pk_f16_fp4 v125, v121, 1.0 op_sel:[1,1,0]
	v_mfma_f32_16x16x32_f16 v[14:17], v[70:73], v[126:129], v[14:17]
	v_cvt_scalef32_pk_f16_fp4 v126, v119, 1.0
	v_cvt_scalef32_pk_f16_fp4 v127, v119, 1.0 op_sel:[1,0,0]
	v_cvt_scalef32_pk_f16_fp4 v128, v119, 1.0 op_sel:[0,1,0]
	v_cvt_scalef32_pk_f16_fp4 v129, v119, 1.0 op_sel:[1,1,0]
	v_mfma_f32_16x16x32_f16 v[10:13], v[78:81], v[122:125], v[10:13]
	v_mfma_f32_16x16x32_f16 v[14:17], v[78:81], v[126:129], v[14:17]
	ds_read_b64_tr_b4 v[118:119], v153 offset:8192
	ds_read_b64_tr_b4 v[120:121], v161 offset:8192
	s_waitcnt lgkmcnt(2)
	v_cvt_scalef32_pk_f16_fp4 v122, v114, 1.0
	v_cvt_scalef32_pk_f16_fp4 v123, v114, 1.0 op_sel:[1,0,0]
	v_cvt_scalef32_pk_f16_fp4 v124, v114, 1.0 op_sel:[0,1,0]
	v_cvt_scalef32_pk_f16_fp4 v125, v114, 1.0 op_sel:[1,1,0]
	v_cvt_scalef32_pk_f16_fp4 v126, v116, 1.0
	v_cvt_scalef32_pk_f16_fp4 v127, v116, 1.0 op_sel:[1,0,0]
	v_cvt_scalef32_pk_f16_fp4 v128, v116, 1.0 op_sel:[0,1,0]
	v_cvt_scalef32_pk_f16_fp4 v129, v116, 1.0 op_sel:[1,1,0]
	v_mfma_f32_16x16x32_f16 v[18:21], v[70:73], v[122:125], v[18:21]
	v_cvt_scalef32_pk_f16_fp4 v122, v117, 1.0
	v_cvt_scalef32_pk_f16_fp4 v123, v117, 1.0 op_sel:[1,0,0]
	v_cvt_scalef32_pk_f16_fp4 v124, v117, 1.0 op_sel:[0,1,0]
	v_cvt_scalef32_pk_f16_fp4 v125, v117, 1.0 op_sel:[1,1,0]
	v_mfma_f32_16x16x32_f16 v[22:25], v[70:73], v[126:129], v[22:25]
	v_cvt_scalef32_pk_f16_fp4 v126, v115, 1.0
	v_cvt_scalef32_pk_f16_fp4 v127, v115, 1.0 op_sel:[1,0,0]
	v_cvt_scalef32_pk_f16_fp4 v128, v115, 1.0 op_sel:[0,1,0]
	v_cvt_scalef32_pk_f16_fp4 v129, v115, 1.0 op_sel:[1,1,0]
	v_mfma_f32_16x16x32_f16 v[18:21], v[78:81], v[122:125], v[18:21]
	v_mfma_f32_16x16x32_f16 v[22:25], v[78:81], v[126:129], v[22:25]
	ds_read_b64_tr_b4 v[114:115], v154 offset:8192
	ds_read_b64_tr_b4 v[116:117], v162 offset:8192
	s_waitcnt lgkmcnt(2)
	v_cvt_scalef32_pk_f16_fp4 v122, v118, 1.0
	v_cvt_scalef32_pk_f16_fp4 v123, v118, 1.0 op_sel:[1,0,0]
	v_cvt_scalef32_pk_f16_fp4 v124, v118, 1.0 op_sel:[0,1,0]
	v_cvt_scalef32_pk_f16_fp4 v125, v118, 1.0 op_sel:[1,1,0]
	v_cvt_scalef32_pk_f16_fp4 v126, v120, 1.0
	v_cvt_scalef32_pk_f16_fp4 v127, v120, 1.0 op_sel:[1,0,0]
	v_cvt_scalef32_pk_f16_fp4 v128, v120, 1.0 op_sel:[0,1,0]
	v_cvt_scalef32_pk_f16_fp4 v129, v120, 1.0 op_sel:[1,1,0]
	v_mfma_f32_16x16x32_f16 v[26:29], v[70:73], v[122:125], v[26:29]
	v_cvt_scalef32_pk_f16_fp4 v122, v121, 1.0
	v_cvt_scalef32_pk_f16_fp4 v123, v121, 1.0 op_sel:[1,0,0]
	v_cvt_scalef32_pk_f16_fp4 v124, v121, 1.0 op_sel:[0,1,0]
	v_cvt_scalef32_pk_f16_fp4 v125, v121, 1.0 op_sel:[1,1,0]
	v_mfma_f32_16x16x32_f16 v[30:33], v[70:73], v[126:129], v[30:33]
	v_cvt_scalef32_pk_f16_fp4 v126, v119, 1.0
	v_cvt_scalef32_pk_f16_fp4 v127, v119, 1.0 op_sel:[1,0,0]
	v_cvt_scalef32_pk_f16_fp4 v128, v119, 1.0 op_sel:[0,1,0]
	v_cvt_scalef32_pk_f16_fp4 v129, v119, 1.0 op_sel:[1,1,0]
	v_mfma_f32_16x16x32_f16 v[26:29], v[78:81], v[122:125], v[26:29]
	v_mfma_f32_16x16x32_f16 v[30:33], v[78:81], v[126:129], v[30:33]
	ds_read_b64_tr_b4 v[118:119], v155 offset:8192
	ds_read_b64_tr_b4 v[120:121], v163 offset:8192
	s_waitcnt lgkmcnt(2)
	v_cvt_scalef32_pk_f16_fp4 v122, v114, 1.0
	v_cvt_scalef32_pk_f16_fp4 v123, v114, 1.0 op_sel:[1,0,0]
	v_cvt_scalef32_pk_f16_fp4 v124, v114, 1.0 op_sel:[0,1,0]
	v_cvt_scalef32_pk_f16_fp4 v125, v114, 1.0 op_sel:[1,1,0]
	v_cvt_scalef32_pk_f16_fp4 v126, v116, 1.0
	v_cvt_scalef32_pk_f16_fp4 v127, v116, 1.0 op_sel:[1,0,0]
	v_cvt_scalef32_pk_f16_fp4 v128, v116, 1.0 op_sel:[0,1,0]
	v_cvt_scalef32_pk_f16_fp4 v129, v116, 1.0 op_sel:[1,1,0]
	v_mfma_f32_16x16x32_f16 v[34:37], v[70:73], v[122:125], v[34:37]
	v_cvt_scalef32_pk_f16_fp4 v122, v117, 1.0
	v_cvt_scalef32_pk_f16_fp4 v123, v117, 1.0 op_sel:[1,0,0]
	v_cvt_scalef32_pk_f16_fp4 v124, v117, 1.0 op_sel:[0,1,0]
	v_cvt_scalef32_pk_f16_fp4 v125, v117, 1.0 op_sel:[1,1,0]
	v_mfma_f32_16x16x32_f16 v[38:41], v[70:73], v[126:129], v[38:41]
	v_cvt_scalef32_pk_f16_fp4 v126, v115, 1.0
	v_cvt_scalef32_pk_f16_fp4 v127, v115, 1.0 op_sel:[1,0,0]
	v_cvt_scalef32_pk_f16_fp4 v128, v115, 1.0 op_sel:[0,1,0]
	v_cvt_scalef32_pk_f16_fp4 v129, v115, 1.0 op_sel:[1,1,0]
	v_mfma_f32_16x16x32_f16 v[34:37], v[78:81], v[122:125], v[34:37]
	v_mfma_f32_16x16x32_f16 v[38:41], v[78:81], v[126:129], v[38:41]
	ds_read_b64_tr_b4 v[114:115], v156 offset:8192
	ds_read_b64_tr_b4 v[116:117], v164 offset:8192
	s_waitcnt lgkmcnt(2)
	v_cvt_scalef32_pk_f16_fp4 v122, v118, 1.0
	v_cvt_scalef32_pk_f16_fp4 v123, v118, 1.0 op_sel:[1,0,0]
	v_cvt_scalef32_pk_f16_fp4 v124, v118, 1.0 op_sel:[0,1,0]
	v_cvt_scalef32_pk_f16_fp4 v125, v118, 1.0 op_sel:[1,1,0]
	v_cvt_scalef32_pk_f16_fp4 v126, v120, 1.0
	v_cvt_scalef32_pk_f16_fp4 v127, v120, 1.0 op_sel:[1,0,0]
	v_cvt_scalef32_pk_f16_fp4 v128, v120, 1.0 op_sel:[0,1,0]
	v_cvt_scalef32_pk_f16_fp4 v129, v120, 1.0 op_sel:[1,1,0]
	v_mfma_f32_16x16x32_f16 v[42:45], v[70:73], v[122:125], v[42:45]
	v_cvt_scalef32_pk_f16_fp4 v122, v121, 1.0
	v_cvt_scalef32_pk_f16_fp4 v123, v121, 1.0 op_sel:[1,0,0]
	v_cvt_scalef32_pk_f16_fp4 v124, v121, 1.0 op_sel:[0,1,0]
	v_cvt_scalef32_pk_f16_fp4 v125, v121, 1.0 op_sel:[1,1,0]
	v_mfma_f32_16x16x32_f16 v[46:49], v[70:73], v[126:129], v[46:49]
	v_cvt_scalef32_pk_f16_fp4 v126, v119, 1.0
	v_cvt_scalef32_pk_f16_fp4 v127, v119, 1.0 op_sel:[1,0,0]
	v_cvt_scalef32_pk_f16_fp4 v128, v119, 1.0 op_sel:[0,1,0]
	v_cvt_scalef32_pk_f16_fp4 v129, v119, 1.0 op_sel:[1,1,0]
	v_mfma_f32_16x16x32_f16 v[42:45], v[78:81], v[122:125], v[42:45]
	v_mfma_f32_16x16x32_f16 v[46:49], v[78:81], v[126:129], v[46:49]
	ds_read_b64_tr_b4 v[118:119], v157 offset:8192
	ds_read_b64_tr_b4 v[120:121], v165 offset:8192
	s_waitcnt lgkmcnt(2)
	v_cvt_scalef32_pk_f16_fp4 v122, v114, 1.0
	v_cvt_scalef32_pk_f16_fp4 v123, v114, 1.0 op_sel:[1,0,0]
	v_cvt_scalef32_pk_f16_fp4 v124, v114, 1.0 op_sel:[0,1,0]
	v_cvt_scalef32_pk_f16_fp4 v125, v114, 1.0 op_sel:[1,1,0]
	v_cvt_scalef32_pk_f16_fp4 v126, v116, 1.0
	v_cvt_scalef32_pk_f16_fp4 v127, v116, 1.0 op_sel:[1,0,0]
	v_cvt_scalef32_pk_f16_fp4 v128, v116, 1.0 op_sel:[0,1,0]
	v_cvt_scalef32_pk_f16_fp4 v129, v116, 1.0 op_sel:[1,1,0]
	v_mfma_f32_16x16x32_f16 v[50:53], v[70:73], v[122:125], v[50:53]
	v_cvt_scalef32_pk_f16_fp4 v122, v117, 1.0
	v_cvt_scalef32_pk_f16_fp4 v123, v117, 1.0 op_sel:[1,0,0]
	v_cvt_scalef32_pk_f16_fp4 v124, v117, 1.0 op_sel:[0,1,0]
	v_cvt_scalef32_pk_f16_fp4 v125, v117, 1.0 op_sel:[1,1,0]
	v_mfma_f32_16x16x32_f16 v[54:57], v[70:73], v[126:129], v[54:57]
	v_cvt_scalef32_pk_f16_fp4 v126, v115, 1.0
	v_cvt_scalef32_pk_f16_fp4 v127, v115, 1.0 op_sel:[1,0,0]
	v_cvt_scalef32_pk_f16_fp4 v128, v115, 1.0 op_sel:[0,1,0]
	v_cvt_scalef32_pk_f16_fp4 v129, v115, 1.0 op_sel:[1,1,0]
	v_mfma_f32_16x16x32_f16 v[50:53], v[78:81], v[122:125], v[50:53]
	v_mfma_f32_16x16x32_f16 v[54:57], v[78:81], v[126:129], v[54:57]
	s_waitcnt vmcnt(0)
	ds_read_b64_tr_b4 v[114:115], v150
	ds_read_b64_tr_b4 v[116:117], v158
	s_waitcnt lgkmcnt(2)
	s_add_i32 m0, s38, 0x2000
	v_mad_u32_u16 v178, v110, v198, v166
	global_load_lds_dwordx4 v178, s[40:41]
	s_add_i32 m0, s38, 0x2400
	v_mad_u32_u16 v179, v110, v198, v167 op_sel:[1,0,0,0]
	global_load_lds_dwordx4 v179, s[40:41]
	s_add_i32 m0, s38, 0x2800
	v_mad_u32_u16 v178, v111, v198, v168
	global_load_lds_dwordx4 v178, s[40:41]
	s_add_i32 m0, s38, 0x2c00
	v_mad_u32_u16 v179, v111, v198, v169 op_sel:[1,0,0,0]
	global_load_lds_dwordx4 v179, s[40:41]
	s_add_i32 m0, s38, 0x3000
	v_mad_u32_u16 v178, v112, v198, v170
	global_load_lds_dwordx4 v178, s[40:41]
	s_add_i32 m0, s38, 0x3400
	v_mad_u32_u16 v179, v112, v198, v171 op_sel:[1,0,0,0]
	global_load_lds_dwordx4 v179, s[40:41]
	s_add_i32 m0, s38, 0x3800
	v_mad_u32_u16 v178, v113, v198, v172
	global_load_lds_dwordx4 v178, s[40:41]
	s_add_i32 m0, s38, 0x3c00
	v_mad_u32_u16 v179, v113, v198, v173 op_sel:[1,0,0,0]
	global_load_lds_dwordx4 v179, s[40:41]
	ds_read_b128 v[82:85], v174 offset:256
	ds_read_b128 v[86:89], v174 offset:272
	ds_read_b128 v[90:93], v175 offset:256
	ds_read_b128 v[94:97], v175 offset:272
	v_cvt_scalef32_pk_f16_fp4 v122, v118, 1.0
	v_cvt_scalef32_pk_f16_fp4 v123, v118, 1.0 op_sel:[1,0,0]
	v_cvt_scalef32_pk_f16_fp4 v124, v118, 1.0 op_sel:[0,1,0]
	v_cvt_scalef32_pk_f16_fp4 v125, v118, 1.0 op_sel:[1,1,0]
	v_cvt_scalef32_pk_f16_fp4 v126, v120, 1.0
	v_cvt_scalef32_pk_f16_fp4 v127, v120, 1.0 op_sel:[1,0,0]
	v_cvt_scalef32_pk_f16_fp4 v128, v120, 1.0 op_sel:[0,1,0]
	v_cvt_scalef32_pk_f16_fp4 v129, v120, 1.0 op_sel:[1,1,0]
	v_mfma_f32_16x16x32_f16 v[58:61], v[70:73], v[122:125], v[58:61]
	v_cvt_scalef32_pk_f16_fp4 v122, v121, 1.0
	v_cvt_scalef32_pk_f16_fp4 v123, v121, 1.0 op_sel:[1,0,0]
	v_cvt_scalef32_pk_f16_fp4 v124, v121, 1.0 op_sel:[0,1,0]
	v_cvt_scalef32_pk_f16_fp4 v125, v121, 1.0 op_sel:[1,1,0]
	v_mfma_f32_16x16x32_f16 v[62:65], v[70:73], v[126:129], v[62:65]
	v_cvt_scalef32_pk_f16_fp4 v126, v119, 1.0
	v_cvt_scalef32_pk_f16_fp4 v127, v119, 1.0 op_sel:[1,0,0]
	v_cvt_scalef32_pk_f16_fp4 v128, v119, 1.0 op_sel:[0,1,0]
	v_cvt_scalef32_pk_f16_fp4 v129, v119, 1.0 op_sel:[1,1,0]
	v_mfma_f32_16x16x32_f16 v[58:61], v[78:81], v[122:125], v[58:61]
	v_mfma_f32_16x16x32_f16 v[62:65], v[78:81], v[126:129], v[62:65]
	s_nop 7
	s_nop 7
	v_cmp_ne_u32_e32 vcc, 0, v196
	v_cndmask_b32_e32 v146, v2, v6, vcc
	v_cndmask_b32_e32 v142, v10, v14, vcc
	v_cndmask_b32_e32 v147, v18, v22, vcc
	v_cndmask_b32_e32 v143, v26, v30, vcc
	v_cndmask_b32_e32 v148, v34, v38, vcc
	v_cndmask_b32_e32 v144, v42, v46, vcc
	v_cndmask_b32_e32 v149, v50, v54, vcc
	v_cndmask_b32_e32 v145, v58, v62, vcc
	v_cmp_ne_u32_e32 vcc, 0, v197
	v_cndmask_b32_e32 v146, v146, v142, vcc
	v_cndmask_b32_e32 v147, v147, v143, vcc
	v_cndmask_b32_e32 v148, v148, v144, vcc
	v_cndmask_b32_e32 v149, v149, v145, vcc
	v_fma_f32 v142, v134, v146, v130
	v_fma_f32 v143, v135, v147, v131
	v_fma_f32 v144, v136, v148, v132
	v_fma_f32 v145, v137, v149, v133
	global_store_dword v[180:181], v142, off
	global_store_dword v[180:181], v143, off offset:256
	global_store_dword v[180:181], v144, off offset:512
	global_store_dword v[180:181], v145, off offset:768
	v_lshl_add_u64 v[180:181], v[180:181], 0, s[48:49]
	s_lshr_b32 s99, s38, 4
	s_add_i32 m0, s99, 0x21000
	s_mov_b64 exec, 0xffff
	global_load_lds_dwordx4 v177, s[0:1]
	s_mov_b64 exec, -1
	v_add_u32_e32 v177, 0x100, v177
	global_load_dwordx4 v[106:109], v176, s[22:23]
	global_load_dwordx4 v[110:113], v176, s[22:23] offset:16
	s_lshl_b32 s99, s43, 8
	s_cmp_eq_u32 s33, 4
	s_cselect_b32 s99, s99, 0x100
	v_add_u32_e32 v176, s99, v176
	global_load_dword v130, v[180:181], off
	global_load_dword v131, v[180:181], off offset:256
	global_load_dword v132, v[180:181], off offset:512
	global_load_dword v133, v[180:181], off offset:768
	ds_read_b64_tr_b4 v[118:119], v151
	ds_read_b64_tr_b4 v[120:121], v159
	s_waitcnt lgkmcnt(2)
	v_cvt_scalef32_pk_f16_fp4 v122, v114, 1.0
	v_cvt_scalef32_pk_f16_fp4 v123, v114, 1.0 op_sel:[1,0,0]
	v_cvt_scalef32_pk_f16_fp4 v124, v114, 1.0 op_sel:[0,1,0]
	v_cvt_scalef32_pk_f16_fp4 v125, v114, 1.0 op_sel:[1,1,0]
	v_cvt_scalef32_pk_f16_fp4 v126, v116, 1.0
	v_cvt_scalef32_pk_f16_fp4 v127, v116, 1.0 op_sel:[1,0,0]
	v_cvt_scalef32_pk_f16_fp4 v128, v116, 1.0 op_sel:[0,1,0]
	v_cvt_scalef32_pk_f16_fp4 v129, v116, 1.0 op_sel:[1,1,0]
	v_mfma_f32_16x16x32_f16 v[2:5], v[82:85], v[122:125], 0
	v_cvt_scalef32_pk_f16_fp4 v122, v117, 1.0
	v_cvt_scalef32_pk_f16_fp4 v123, v117, 1.0 op_sel:[1,0,0]
	v_cvt_scalef32_pk_f16_fp4 v124, v117, 1.0 op_sel:[0,1,0]
	v_cvt_scalef32_pk_f16_fp4 v125, v117, 1.0 op_sel:[1,1,0]
	v_mfma_f32_16x16x32_f16 v[6:9], v[82:85], v[126:129], 0
	v_cvt_scalef32_pk_f16_fp4 v126, v115, 1.0
	v_cvt_scalef32_pk_f16_fp4 v127, v115, 1.0 op_sel:[1,0,0]
	v_cvt_scalef32_pk_f16_fp4 v128, v115, 1.0 op_sel:[0,1,0]
	v_cvt_scalef32_pk_f16_fp4 v129, v115, 1.0 op_sel:[1,1,0]
	v_mfma_f32_16x16x32_f16 v[2:5], v[90:93], v[122:125], v[2:5]
	v_mfma_f32_16x16x32_f16 v[6:9], v[90:93], v[126:129], v[6:9]
	ds_read_b64_tr_b4 v[114:115], v152
	ds_read_b64_tr_b4 v[116:117], v160
	s_waitcnt lgkmcnt(2)
	v_cvt_scalef32_pk_f16_fp4 v122, v118, 1.0
	v_cvt_scalef32_pk_f16_fp4 v123, v118, 1.0 op_sel:[1,0,0]
	v_cvt_scalef32_pk_f16_fp4 v124, v118, 1.0 op_sel:[0,1,0]
	v_cvt_scalef32_pk_f16_fp4 v125, v118, 1.0 op_sel:[1,1,0]
	v_cvt_scalef32_pk_f16_fp4 v126, v120, 1.0
	v_cvt_scalef32_pk_f16_fp4 v127, v120, 1.0 op_sel:[1,0,0]
	v_cvt_scalef32_pk_f16_fp4 v128, v120, 1.0 op_sel:[0,1,0]
	v_cvt_scalef32_pk_f16_fp4 v129, v120, 1.0 op_sel:[1,1,0]
	v_mfma_f32_16x16x32_f16 v[10:13], v[82:85], v[122:125], 0
	v_cvt_scalef32_pk_f16_fp4 v122, v121, 1.0
	v_cvt_scalef32_pk_f16_fp4 v123, v121, 1.0 op_sel:[1,0,0]
	v_cvt_scalef32_pk_f16_fp4 v124, v121, 1.0 op_sel:[0,1,0]
	v_cvt_scalef32_pk_f16_fp4 v125, v121, 1.0 op_sel:[1,1,0]
	v_mfma_f32_16x16x32_f16 v[14:17], v[82:85], v[126:129], 0
	v_cvt_scalef32_pk_f16_fp4 v126, v119, 1.0
	v_cvt_scalef32_pk_f16_fp4 v127, v119, 1.0 op_sel:[1,0,0]
	v_cvt_scalef32_pk_f16_fp4 v128, v119, 1.0 op_sel:[0,1,0]
	v_cvt_scalef32_pk_f16_fp4 v129, v119, 1.0 op_sel:[1,1,0]
	v_mfma_f32_16x16x32_f16 v[10:13], v[90:93], v[122:125], v[10:13]
	v_mfma_f32_16x16x32_f16 v[14:17], v[90:93], v[126:129], v[14:17]
	ds_read_b64_tr_b4 v[118:119], v153
	ds_read_b64_tr_b4 v[120:121], v161
	s_waitcnt lgkmcnt(2)
	v_cvt_scalef32_pk_f16_fp4 v122, v114, 1.0
	v_cvt_scalef32_pk_f16_fp4 v123, v114, 1.0 op_sel:[1,0,0]
	v_cvt_scalef32_pk_f16_fp4 v124, v114, 1.0 op_sel:[0,1,0]
	v_cvt_scalef32_pk_f16_fp4 v125, v114, 1.0 op_sel:[1,1,0]
	v_cvt_scalef32_pk_f16_fp4 v126, v116, 1.0
	v_cvt_scalef32_pk_f16_fp4 v127, v116, 1.0 op_sel:[1,0,0]
	v_cvt_scalef32_pk_f16_fp4 v128, v116, 1.0 op_sel:[0,1,0]
	v_cvt_scalef32_pk_f16_fp4 v129, v116, 1.0 op_sel:[1,1,0]
	v_mfma_f32_16x16x32_f16 v[18:21], v[82:85], v[122:125], 0
	v_cvt_scalef32_pk_f16_fp4 v122, v117, 1.0
	v_cvt_scalef32_pk_f16_fp4 v123, v117, 1.0 op_sel:[1,0,0]
	v_cvt_scalef32_pk_f16_fp4 v124, v117, 1.0 op_sel:[0,1,0]
	v_cvt_scalef32_pk_f16_fp4 v125, v117, 1.0 op_sel:[1,1,0]
	v_mfma_f32_16x16x32_f16 v[22:25], v[82:85], v[126:129], 0
	v_cvt_scalef32_pk_f16_fp4 v126, v115, 1.0
	v_cvt_scalef32_pk_f16_fp4 v127, v115, 1.0 op_sel:[1,0,0]
	v_cvt_scalef32_pk_f16_fp4 v128, v115, 1.0 op_sel:[0,1,0]
	v_cvt_scalef32_pk_f16_fp4 v129, v115, 1.0 op_sel:[1,1,0]
	v_mfma_f32_16x16x32_f16 v[18:21], v[90:93], v[122:125], v[18:21]
	v_mfma_f32_16x16x32_f16 v[22:25], v[90:93], v[126:129], v[22:25]
	ds_read_b64_tr_b4 v[114:115], v154
	ds_read_b64_tr_b4 v[116:117], v162
	s_waitcnt lgkmcnt(2)
	v_cvt_scalef32_pk_f16_fp4 v122, v118, 1.0
	v_cvt_scalef32_pk_f16_fp4 v123, v118, 1.0 op_sel:[1,0,0]
	v_cvt_scalef32_pk_f16_fp4 v124, v118, 1.0 op_sel:[0,1,0]
	v_cvt_scalef32_pk_f16_fp4 v125, v118, 1.0 op_sel:[1,1,0]
	v_cvt_scalef32_pk_f16_fp4 v126, v120, 1.0
	v_cvt_scalef32_pk_f16_fp4 v127, v120, 1.0 op_sel:[1,0,0]
	v_cvt_scalef32_pk_f16_fp4 v128, v120, 1.0 op_sel:[0,1,0]
	v_cvt_scalef32_pk_f16_fp4 v129, v120, 1.0 op_sel:[1,1,0]
	v_mfma_f32_16x16x32_f16 v[26:29], v[82:85], v[122:125], 0
	v_cvt_scalef32_pk_f16_fp4 v122, v121, 1.0
	v_cvt_scalef32_pk_f16_fp4 v123, v121, 1.0 op_sel:[1,0,0]
	v_cvt_scalef32_pk_f16_fp4 v124, v121, 1.0 op_sel:[0,1,0]
	v_cvt_scalef32_pk_f16_fp4 v125, v121, 1.0 op_sel:[1,1,0]
	v_mfma_f32_16x16x32_f16 v[30:33], v[82:85], v[126:129], 0
	v_cvt_scalef32_pk_f16_fp4 v126, v119, 1.0
	v_cvt_scalef32_pk_f16_fp4 v127, v119, 1.0 op_sel:[1,0,0]
	v_cvt_scalef32_pk_f16_fp4 v128, v119, 1.0 op_sel:[0,1,0]
	v_cvt_scalef32_pk_f16_fp4 v129, v119, 1.0 op_sel:[1,1,0]
	v_mfma_f32_16x16x32_f16 v[26:29], v[90:93], v[122:125], v[26:29]
	v_mfma_f32_16x16x32_f16 v[30:33], v[90:93], v[126:129], v[30:33]
	ds_read_b64_tr_b4 v[118:119], v155
	ds_read_b64_tr_b4 v[120:121], v163
	s_waitcnt lgkmcnt(2)
	v_cvt_scalef32_pk_f16_fp4 v122, v114, 1.0
	v_cvt_scalef32_pk_f16_fp4 v123, v114, 1.0 op_sel:[1,0,0]
	v_cvt_scalef32_pk_f16_fp4 v124, v114, 1.0 op_sel:[0,1,0]
	v_cvt_scalef32_pk_f16_fp4 v125, v114, 1.0 op_sel:[1,1,0]
	v_cvt_scalef32_pk_f16_fp4 v126, v116, 1.0
	v_cvt_scalef32_pk_f16_fp4 v127, v116, 1.0 op_sel:[1,0,0]
	v_cvt_scalef32_pk_f16_fp4 v128, v116, 1.0 op_sel:[0,1,0]
	v_cvt_scalef32_pk_f16_fp4 v129, v116, 1.0 op_sel:[1,1,0]
	v_mfma_f32_16x16x32_f16 v[34:37], v[82:85], v[122:125], 0
	v_cvt_scalef32_pk_f16_fp4 v122, v117, 1.0
	v_cvt_scalef32_pk_f16_fp4 v123, v117, 1.0 op_sel:[1,0,0]
	v_cvt_scalef32_pk_f16_fp4 v124, v117, 1.0 op_sel:[0,1,0]
	v_cvt_scalef32_pk_f16_fp4 v125, v117, 1.0 op_sel:[1,1,0]
	v_mfma_f32_16x16x32_f16 v[38:41], v[82:85], v[126:129], 0
	v_cvt_scalef32_pk_f16_fp4 v126, v115, 1.0
	v_cvt_scalef32_pk_f16_fp4 v127, v115, 1.0 op_sel:[1,0,0]
	v_cvt_scalef32_pk_f16_fp4 v128, v115, 1.0 op_sel:[0,1,0]
	v_cvt_scalef32_pk_f16_fp4 v129, v115, 1.0 op_sel:[1,1,0]
	v_mfma_f32_16x16x32_f16 v[34:37], v[90:93], v[122:125], v[34:37]
	v_mfma_f32_16x16x32_f16 v[38:41], v[90:93], v[126:129], v[38:41]
	ds_read_b64_tr_b4 v[114:115], v156
	ds_read_b64_tr_b4 v[116:117], v164
	s_waitcnt lgkmcnt(2)
	v_cvt_scalef32_pk_f16_fp4 v122, v118, 1.0
	v_cvt_scalef32_pk_f16_fp4 v123, v118, 1.0 op_sel:[1,0,0]
	v_cvt_scalef32_pk_f16_fp4 v124, v118, 1.0 op_sel:[0,1,0]
	v_cvt_scalef32_pk_f16_fp4 v125, v118, 1.0 op_sel:[1,1,0]
	v_cvt_scalef32_pk_f16_fp4 v126, v120, 1.0
	v_cvt_scalef32_pk_f16_fp4 v127, v120, 1.0 op_sel:[1,0,0]
	v_cvt_scalef32_pk_f16_fp4 v128, v120, 1.0 op_sel:[0,1,0]
	v_cvt_scalef32_pk_f16_fp4 v129, v120, 1.0 op_sel:[1,1,0]
	v_mfma_f32_16x16x32_f16 v[42:45], v[82:85], v[122:125], 0
	v_cvt_scalef32_pk_f16_fp4 v122, v121, 1.0
	v_cvt_scalef32_pk_f16_fp4 v123, v121, 1.0 op_sel:[1,0,0]
	v_cvt_scalef32_pk_f16_fp4 v124, v121, 1.0 op_sel:[0,1,0]
	v_cvt_scalef32_pk_f16_fp4 v125, v121, 1.0 op_sel:[1,1,0]
	v_mfma_f32_16x16x32_f16 v[46:49], v[82:85], v[126:129], 0
	v_cvt_scalef32_pk_f16_fp4 v126, v119, 1.0
	v_cvt_scalef32_pk_f16_fp4 v127, v119, 1.0 op_sel:[1,0,0]
	v_cvt_scalef32_pk_f16_fp4 v128, v119, 1.0 op_sel:[0,1,0]
	v_cvt_scalef32_pk_f16_fp4 v129, v119, 1.0 op_sel:[1,1,0]
	v_mfma_f32_16x16x32_f16 v[42:45], v[90:93], v[122:125], v[42:45]
	v_mfma_f32_16x16x32_f16 v[46:49], v[90:93], v[126:129], v[46:49]
	ds_read_b64_tr_b4 v[118:119], v157
	ds_read_b64_tr_b4 v[120:121], v165
	s_waitcnt lgkmcnt(2)
	v_cvt_scalef32_pk_f16_fp4 v122, v114, 1.0
	v_cvt_scalef32_pk_f16_fp4 v123, v114, 1.0 op_sel:[1,0,0]
	v_cvt_scalef32_pk_f16_fp4 v124, v114, 1.0 op_sel:[0,1,0]
	v_cvt_scalef32_pk_f16_fp4 v125, v114, 1.0 op_sel:[1,1,0]
	v_cvt_scalef32_pk_f16_fp4 v126, v116, 1.0
	v_cvt_scalef32_pk_f16_fp4 v127, v116, 1.0 op_sel:[1,0,0]
	v_cvt_scalef32_pk_f16_fp4 v128, v116, 1.0 op_sel:[0,1,0]
	v_cvt_scalef32_pk_f16_fp4 v129, v116, 1.0 op_sel:[1,1,0]
	v_mfma_f32_16x16x32_f16 v[50:53], v[82:85], v[122:125], 0
	v_cvt_scalef32_pk_f16_fp4 v122, v117, 1.0
	v_cvt_scalef32_pk_f16_fp4 v123, v117, 1.0 op_sel:[1,0,0]
	v_cvt_scalef32_pk_f16_fp4 v124, v117, 1.0 op_sel:[0,1,0]
	v_cvt_scalef32_pk_f16_fp4 v125, v117, 1.0 op_sel:[1,1,0]
	v_mfma_f32_16x16x32_f16 v[54:57], v[82:85], v[126:129], 0
	v_cvt_scalef32_pk_f16_fp4 v126, v115, 1.0
	v_cvt_scalef32_pk_f16_fp4 v127, v115, 1.0 op_sel:[1,0,0]
	v_cvt_scalef32_pk_f16_fp4 v128, v115, 1.0 op_sel:[0,1,0]
	v_cvt_scalef32_pk_f16_fp4 v129, v115, 1.0 op_sel:[1,1,0]
	v_mfma_f32_16x16x32_f16 v[50:53], v[90:93], v[122:125], v[50:53]
	v_mfma_f32_16x16x32_f16 v[54:57], v[90:93], v[126:129], v[54:57]
	s_waitcnt vmcnt(11)
	ds_read_b64_tr_b4 v[114:115], v150 offset:8192
	ds_read_b64_tr_b4 v[116:117], v158 offset:8192
	s_waitcnt lgkmcnt(2)
	s_add_i32 m0, s38, 0x0
	v_mad_u32_u16 v178, v98, v198, v166
	global_load_lds_dwordx4 v178, s[40:41]
	s_add_i32 m0, s38, 0x400
	v_mad_u32_u16 v179, v98, v198, v167 op_sel:[1,0,0,0]
	global_load_lds_dwordx4 v179, s[40:41]
	s_add_i32 m0, s38, 0x800
	v_mad_u32_u16 v178, v99, v198, v168
	global_load_lds_dwordx4 v178, s[40:41]
	s_add_i32 m0, s38, 0xc00
	v_mad_u32_u16 v179, v99, v198, v169 op_sel:[1,0,0,0]
	global_load_lds_dwordx4 v179, s[40:41]
	s_add_i32 m0, s38, 0x1000
	v_mad_u32_u16 v178, v100, v198, v170
	global_load_lds_dwordx4 v178, s[40:41]
	s_add_i32 m0, s38, 0x1400
	v_mad_u32_u16 v179, v100, v198, v171 op_sel:[1,0,0,0]
	global_load_lds_dwordx4 v179, s[40:41]
	s_add_i32 m0, s38, 0x1800
	v_mad_u32_u16 v178, v101, v198, v172
	global_load_lds_dwordx4 v178, s[40:41]
	s_add_i32 m0, s38, 0x1c00
	v_mad_u32_u16 v179, v101, v198, v173 op_sel:[1,0,0,0]
	global_load_lds_dwordx4 v179, s[40:41]
	v_cvt_scalef32_pk_f16_fp4 v122, v118, 1.0
	v_cvt_scalef32_pk_f16_fp4 v123, v118, 1.0 op_sel:[1,0,0]
	v_cvt_scalef32_pk_f16_fp4 v124, v118, 1.0 op_sel:[0,1,0]
	v_cvt_scalef32_pk_f16_fp4 v125, v118, 1.0 op_sel:[1,1,0]
	v_cvt_scalef32_pk_f16_fp4 v126, v120, 1.0
	v_cvt_scalef32_pk_f16_fp4 v127, v120, 1.0 op_sel:[1,0,0]
	v_cvt_scalef32_pk_f16_fp4 v128, v120, 1.0 op_sel:[0,1,0]
	v_cvt_scalef32_pk_f16_fp4 v129, v120, 1.0 op_sel:[1,1,0]
	v_mfma_f32_16x16x32_f16 v[58:61], v[82:85], v[122:125], 0
	v_cvt_scalef32_pk_f16_fp4 v122, v121, 1.0
	v_cvt_scalef32_pk_f16_fp4 v123, v121, 1.0 op_sel:[1,0,0]
	v_cvt_scalef32_pk_f16_fp4 v124, v121, 1.0 op_sel:[0,1,0]
	v_cvt_scalef32_pk_f16_fp4 v125, v121, 1.0 op_sel:[1,1,0]
	v_mfma_f32_16x16x32_f16 v[62:65], v[82:85], v[126:129], 0
	v_cvt_scalef32_pk_f16_fp4 v126, v119, 1.0
	v_cvt_scalef32_pk_f16_fp4 v127, v119, 1.0 op_sel:[1,0,0]
	v_cvt_scalef32_pk_f16_fp4 v128, v119, 1.0 op_sel:[0,1,0]
	v_cvt_scalef32_pk_f16_fp4 v129, v119, 1.0 op_sel:[1,1,0]
	v_mfma_f32_16x16x32_f16 v[58:61], v[90:93], v[122:125], v[58:61]
	v_mfma_f32_16x16x32_f16 v[62:65], v[90:93], v[126:129], v[62:65]
	ds_read_b64_tr_b4 v[118:119], v151 offset:8192
	ds_read_b64_tr_b4 v[120:121], v159 offset:8192
	s_waitcnt lgkmcnt(2)
	v_cvt_scalef32_pk_f16_fp4 v122, v114, 1.0
	v_cvt_scalef32_pk_f16_fp4 v123, v114, 1.0 op_sel:[1,0,0]
	v_cvt_scalef32_pk_f16_fp4 v124, v114, 1.0 op_sel:[0,1,0]
	v_cvt_scalef32_pk_f16_fp4 v125, v114, 1.0 op_sel:[1,1,0]
	v_cvt_scalef32_pk_f16_fp4 v126, v116, 1.0
	v_cvt_scalef32_pk_f16_fp4 v127, v116, 1.0 op_sel:[1,0,0]
	v_cvt_scalef32_pk_f16_fp4 v128, v116, 1.0 op_sel:[0,1,0]
	v_cvt_scalef32_pk_f16_fp4 v129, v116, 1.0 op_sel:[1,1,0]
	v_mfma_f32_16x16x32_f16 v[2:5], v[86:89], v[122:125], v[2:5]
	v_cvt_scalef32_pk_f16_fp4 v122, v117, 1.0
	v_cvt_scalef32_pk_f16_fp4 v123, v117, 1.0 op_sel:[1,0,0]
	v_cvt_scalef32_pk_f16_fp4 v124, v117, 1.0 op_sel:[0,1,0]
	v_cvt_scalef32_pk_f16_fp4 v125, v117, 1.0 op_sel:[1,1,0]
	v_mfma_f32_16x16x32_f16 v[6:9], v[86:89], v[126:129], v[6:9]
	v_cvt_scalef32_pk_f16_fp4 v126, v115, 1.0
	v_cvt_scalef32_pk_f16_fp4 v127, v115, 1.0 op_sel:[1,0,0]
	v_cvt_scalef32_pk_f16_fp4 v128, v115, 1.0 op_sel:[0,1,0]
	v_cvt_scalef32_pk_f16_fp4 v129, v115, 1.0 op_sel:[1,1,0]
	v_mfma_f32_16x16x32_f16 v[2:5], v[94:97], v[122:125], v[2:5]
	v_mfma_f32_16x16x32_f16 v[6:9], v[94:97], v[126:129], v[6:9]
	ds_read_b64_tr_b4 v[114:115], v152 offset:8192
	ds_read_b64_tr_b4 v[116:117], v160 offset:8192
	s_waitcnt lgkmcnt(2)
	v_cvt_scalef32_pk_f16_fp4 v122, v118, 1.0
	v_cvt_scalef32_pk_f16_fp4 v123, v118, 1.0 op_sel:[1,0,0]
	v_cvt_scalef32_pk_f16_fp4 v124, v118, 1.0 op_sel:[0,1,0]
	v_cvt_scalef32_pk_f16_fp4 v125, v118, 1.0 op_sel:[1,1,0]
	v_cvt_scalef32_pk_f16_fp4 v126, v120, 1.0
	v_cvt_scalef32_pk_f16_fp4 v127, v120, 1.0 op_sel:[1,0,0]
	v_cvt_scalef32_pk_f16_fp4 v128, v120, 1.0 op_sel:[0,1,0]
	v_cvt_scalef32_pk_f16_fp4 v129, v120, 1.0 op_sel:[1,1,0]
	v_mfma_f32_16x16x32_f16 v[10:13], v[86:89], v[122:125], v[10:13]
	v_cvt_scalef32_pk_f16_fp4 v122, v121, 1.0
	v_cvt_scalef32_pk_f16_fp4 v123, v121, 1.0 op_sel:[1,0,0]
	v_cvt_scalef32_pk_f16_fp4 v124, v121, 1.0 op_sel:[0,1,0]
	v_cvt_scalef32_pk_f16_fp4 v125, v121, 1.0 op_sel:[1,1,0]
	v_mfma_f32_16x16x32_f16 v[14:17], v[86:89], v[126:129], v[14:17]
	v_cvt_scalef32_pk_f16_fp4 v126, v119, 1.0
	v_cvt_scalef32_pk_f16_fp4 v127, v119, 1.0 op_sel:[1,0,0]
	v_cvt_scalef32_pk_f16_fp4 v128, v119, 1.0 op_sel:[0,1,0]
	v_cvt_scalef32_pk_f16_fp4 v129, v119, 1.0 op_sel:[1,1,0]
	v_mfma_f32_16x16x32_f16 v[10:13], v[94:97], v[122:125], v[10:13]
	v_mfma_f32_16x16x32_f16 v[14:17], v[94:97], v[126:129], v[14:17]
	ds_read_b64_tr_b4 v[118:119], v153 offset:8192
	ds_read_b64_tr_b4 v[120:121], v161 offset:8192
	s_waitcnt lgkmcnt(2)
	v_cvt_scalef32_pk_f16_fp4 v122, v114, 1.0
	v_cvt_scalef32_pk_f16_fp4 v123, v114, 1.0 op_sel:[1,0,0]
	v_cvt_scalef32_pk_f16_fp4 v124, v114, 1.0 op_sel:[0,1,0]
	v_cvt_scalef32_pk_f16_fp4 v125, v114, 1.0 op_sel:[1,1,0]
	v_cvt_scalef32_pk_f16_fp4 v126, v116, 1.0
	v_cvt_scalef32_pk_f16_fp4 v127, v116, 1.0 op_sel:[1,0,0]
	v_cvt_scalef32_pk_f16_fp4 v128, v116, 1.0 op_sel:[0,1,0]
	v_cvt_scalef32_pk_f16_fp4 v129, v116, 1.0 op_sel:[1,1,0]
	v_mfma_f32_16x16x32_f16 v[18:21], v[86:89], v[122:125], v[18:21]
	v_cvt_scalef32_pk_f16_fp4 v122, v117, 1.0
	v_cvt_scalef32_pk_f16_fp4 v123, v117, 1.0 op_sel:[1,0,0]
	v_cvt_scalef32_pk_f16_fp4 v124, v117, 1.0 op_sel:[0,1,0]
	v_cvt_scalef32_pk_f16_fp4 v125, v117, 1.0 op_sel:[1,1,0]
	v_mfma_f32_16x16x32_f16 v[22:25], v[86:89], v[126:129], v[22:25]
	v_cvt_scalef32_pk_f16_fp4 v126, v115, 1.0
	v_cvt_scalef32_pk_f16_fp4 v127, v115, 1.0 op_sel:[1,0,0]
	v_cvt_scalef32_pk_f16_fp4 v128, v115, 1.0 op_sel:[0,1,0]
	v_cvt_scalef32_pk_f16_fp4 v129, v115, 1.0 op_sel:[1,1,0]
	v_mfma_f32_16x16x32_f16 v[18:21], v[94:97], v[122:125], v[18:21]
	v_mfma_f32_16x16x32_f16 v[22:25], v[94:97], v[126:129], v[22:25]
	ds_read_b64_tr_b4 v[114:115], v154 offset:8192
	ds_read_b64_tr_b4 v[116:117], v162 offset:8192
	s_waitcnt lgkmcnt(2)
	v_cvt_scalef32_pk_f16_fp4 v122, v118, 1.0
	v_cvt_scalef32_pk_f16_fp4 v123, v118, 1.0 op_sel:[1,0,0]
	v_cvt_scalef32_pk_f16_fp4 v124, v118, 1.0 op_sel:[0,1,0]
	v_cvt_scalef32_pk_f16_fp4 v125, v118, 1.0 op_sel:[1,1,0]
	v_cvt_scalef32_pk_f16_fp4 v126, v120, 1.0
	v_cvt_scalef32_pk_f16_fp4 v127, v120, 1.0 op_sel:[1,0,0]
	v_cvt_scalef32_pk_f16_fp4 v128, v120, 1.0 op_sel:[0,1,0]
	v_cvt_scalef32_pk_f16_fp4 v129, v120, 1.0 op_sel:[1,1,0]
	v_mfma_f32_16x16x32_f16 v[26:29], v[86:89], v[122:125], v[26:29]
	v_cvt_scalef32_pk_f16_fp4 v122, v121, 1.0
	v_cvt_scalef32_pk_f16_fp4 v123, v121, 1.0 op_sel:[1,0,0]
	v_cvt_scalef32_pk_f16_fp4 v124, v121, 1.0 op_sel:[0,1,0]
	v_cvt_scalef32_pk_f16_fp4 v125, v121, 1.0 op_sel:[1,1,0]
	v_mfma_f32_16x16x32_f16 v[30:33], v[86:89], v[126:129], v[30:33]
	v_cvt_scalef32_pk_f16_fp4 v126, v119, 1.0
	v_cvt_scalef32_pk_f16_fp4 v127, v119, 1.0 op_sel:[1,0,0]
	v_cvt_scalef32_pk_f16_fp4 v128, v119, 1.0 op_sel:[0,1,0]
	v_cvt_scalef32_pk_f16_fp4 v129, v119, 1.0 op_sel:[1,1,0]
	v_mfma_f32_16x16x32_f16 v[26:29], v[94:97], v[122:125], v[26:29]
	v_mfma_f32_16x16x32_f16 v[30:33], v[94:97], v[126:129], v[30:33]
	ds_read_b64_tr_b4 v[118:119], v155 offset:8192
	ds_read_b64_tr_b4 v[120:121], v163 offset:8192
	s_waitcnt lgkmcnt(2)
	v_cvt_scalef32_pk_f16_fp4 v122, v114, 1.0
	v_cvt_scalef32_pk_f16_fp4 v123, v114, 1.0 op_sel:[1,0,0]
	v_cvt_scalef32_pk_f16_fp4 v124, v114, 1.0 op_sel:[0,1,0]
	v_cvt_scalef32_pk_f16_fp4 v125, v114, 1.0 op_sel:[1,1,0]
	v_cvt_scalef32_pk_f16_fp4 v126, v116, 1.0
	v_cvt_scalef32_pk_f16_fp4 v127, v116, 1.0 op_sel:[1,0,0]
	v_cvt_scalef32_pk_f16_fp4 v128, v116, 1.0 op_sel:[0,1,0]
	v_cvt_scalef32_pk_f16_fp4 v129, v116, 1.0 op_sel:[1,1,0]
	v_mfma_f32_16x16x32_f16 v[34:37], v[86:89], v[122:125], v[34:37]
	v_cvt_scalef32_pk_f16_fp4 v122, v117, 1.0
	v_cvt_scalef32_pk_f16_fp4 v123, v117, 1.0 op_sel:[1,0,0]
	v_cvt_scalef32_pk_f16_fp4 v124, v117, 1.0 op_sel:[0,1,0]
	v_cvt_scalef32_pk_f16_fp4 v125, v117, 1.0 op_sel:[1,1,0]
	v_mfma_f32_16x16x32_f16 v[38:41], v[86:89], v[126:129], v[38:41]
	v_cvt_scalef32_pk_f16_fp4 v126, v115, 1.0
	v_cvt_scalef32_pk_f16_fp4 v127, v115, 1.0 op_sel:[1,0,0]
	v_cvt_scalef32_pk_f16_fp4 v128, v115, 1.0 op_sel:[0,1,0]
	v_cvt_scalef32_pk_f16_fp4 v129, v115, 1.0 op_sel:[1,1,0]
	v_mfma_f32_16x16x32_f16 v[34:37], v[94:97], v[122:125], v[34:37]
	v_mfma_f32_16x16x32_f16 v[38:41], v[94:97], v[126:129], v[38:41]
	ds_read_b64_tr_b4 v[114:115], v156 offset:8192
	ds_read_b64_tr_b4 v[116:117], v164 offset:8192
	s_waitcnt lgkmcnt(2)
	v_cvt_scalef32_pk_f16_fp4 v122, v118, 1.0
	v_cvt_scalef32_pk_f16_fp4 v123, v118, 1.0 op_sel:[1,0,0]
	v_cvt_scalef32_pk_f16_fp4 v124, v118, 1.0 op_sel:[0,1,0]
	v_cvt_scalef32_pk_f16_fp4 v125, v118, 1.0 op_sel:[1,1,0]
	v_cvt_scalef32_pk_f16_fp4 v126, v120, 1.0
	v_cvt_scalef32_pk_f16_fp4 v127, v120, 1.0 op_sel:[1,0,0]
	v_cvt_scalef32_pk_f16_fp4 v128, v120, 1.0 op_sel:[0,1,0]
	v_cvt_scalef32_pk_f16_fp4 v129, v120, 1.0 op_sel:[1,1,0]
	v_mfma_f32_16x16x32_f16 v[42:45], v[86:89], v[122:125], v[42:45]
	v_cvt_scalef32_pk_f16_fp4 v122, v121, 1.0
	v_cvt_scalef32_pk_f16_fp4 v123, v121, 1.0 op_sel:[1,0,0]
	v_cvt_scalef32_pk_f16_fp4 v124, v121, 1.0 op_sel:[0,1,0]
	v_cvt_scalef32_pk_f16_fp4 v125, v121, 1.0 op_sel:[1,1,0]
	v_mfma_f32_16x16x32_f16 v[46:49], v[86:89], v[126:129], v[46:49]
	v_cvt_scalef32_pk_f16_fp4 v126, v119, 1.0
	v_cvt_scalef32_pk_f16_fp4 v127, v119, 1.0 op_sel:[1,0,0]
	v_cvt_scalef32_pk_f16_fp4 v128, v119, 1.0 op_sel:[0,1,0]
	v_cvt_scalef32_pk_f16_fp4 v129, v119, 1.0 op_sel:[1,1,0]
	v_mfma_f32_16x16x32_f16 v[42:45], v[94:97], v[122:125], v[42:45]
	v_mfma_f32_16x16x32_f16 v[46:49], v[94:97], v[126:129], v[46:49]
	ds_read_b64_tr_b4 v[118:119], v157 offset:8192
	ds_read_b64_tr_b4 v[120:121], v165 offset:8192
	s_waitcnt lgkmcnt(2)
	v_cvt_scalef32_pk_f16_fp4 v122, v114, 1.0
	v_cvt_scalef32_pk_f16_fp4 v123, v114, 1.0 op_sel:[1,0,0]
	v_cvt_scalef32_pk_f16_fp4 v124, v114, 1.0 op_sel:[0,1,0]
	v_cvt_scalef32_pk_f16_fp4 v125, v114, 1.0 op_sel:[1,1,0]
	v_cvt_scalef32_pk_f16_fp4 v126, v116, 1.0
	v_cvt_scalef32_pk_f16_fp4 v127, v116, 1.0 op_sel:[1,0,0]
	v_cvt_scalef32_pk_f16_fp4 v128, v116, 1.0 op_sel:[0,1,0]
	v_cvt_scalef32_pk_f16_fp4 v129, v116, 1.0 op_sel:[1,1,0]
	v_mfma_f32_16x16x32_f16 v[50:53], v[86:89], v[122:125], v[50:53]
	v_cvt_scalef32_pk_f16_fp4 v122, v117, 1.0
	v_cvt_scalef32_pk_f16_fp4 v123, v117, 1.0 op_sel:[1,0,0]
	v_cvt_scalef32_pk_f16_fp4 v124, v117, 1.0 op_sel:[0,1,0]
	v_cvt_scalef32_pk_f16_fp4 v125, v117, 1.0 op_sel:[1,1,0]
	v_mfma_f32_16x16x32_f16 v[54:57], v[86:89], v[126:129], v[54:57]
	v_cvt_scalef32_pk_f16_fp4 v126, v115, 1.0
	v_cvt_scalef32_pk_f16_fp4 v127, v115, 1.0 op_sel:[1,0,0]
	v_cvt_scalef32_pk_f16_fp4 v128, v115, 1.0 op_sel:[0,1,0]
	v_cvt_scalef32_pk_f16_fp4 v129, v115, 1.0 op_sel:[1,1,0]
	v_mfma_f32_16x16x32_f16 v[50:53], v[94:97], v[122:125], v[50:53]
	v_mfma_f32_16x16x32_f16 v[54:57], v[94:97], v[126:129], v[54:57]
	s_waitcnt vmcnt(0)
	ds_read_b64_tr_b4 v[114:115], v150
	ds_read_b64_tr_b4 v[116:117], v158
	s_waitcnt lgkmcnt(2)
	s_add_i32 m0, s38, 0x2000
	v_mad_u32_u16 v178, v102, v198, v166
	global_load_lds_dwordx4 v178, s[40:41]
	s_add_i32 m0, s38, 0x2400
	v_mad_u32_u16 v179, v102, v198, v167 op_sel:[1,0,0,0]
	global_load_lds_dwordx4 v179, s[40:41]
	s_add_i32 m0, s38, 0x2800
	v_mad_u32_u16 v178, v103, v198, v168
	global_load_lds_dwordx4 v178, s[40:41]
	s_add_i32 m0, s38, 0x2c00
	v_mad_u32_u16 v179, v103, v198, v169 op_sel:[1,0,0,0]
	global_load_lds_dwordx4 v179, s[40:41]
	s_add_i32 m0, s38, 0x3000
	v_mad_u32_u16 v178, v104, v198, v170
	global_load_lds_dwordx4 v178, s[40:41]
	s_add_i32 m0, s38, 0x3400
	v_mad_u32_u16 v179, v104, v198, v171 op_sel:[1,0,0,0]
	global_load_lds_dwordx4 v179, s[40:41]
	s_add_i32 m0, s38, 0x3800
	v_mad_u32_u16 v178, v105, v198, v172
	global_load_lds_dwordx4 v178, s[40:41]
	s_add_i32 m0, s38, 0x3c00
	v_mad_u32_u16 v179, v105, v198, v173 op_sel:[1,0,0,0]
	global_load_lds_dwordx4 v179, s[40:41]
	ds_read_b128 v[66:69], v174
	ds_read_b128 v[70:73], v174 offset:16
	ds_read_b128 v[74:77], v175
	ds_read_b128 v[78:81], v175 offset:16
	v_cvt_scalef32_pk_f16_fp4 v122, v118, 1.0
	v_cvt_scalef32_pk_f16_fp4 v123, v118, 1.0 op_sel:[1,0,0]
	v_cvt_scalef32_pk_f16_fp4 v124, v118, 1.0 op_sel:[0,1,0]
	v_cvt_scalef32_pk_f16_fp4 v125, v118, 1.0 op_sel:[1,1,0]
	v_cvt_scalef32_pk_f16_fp4 v126, v120, 1.0
	v_cvt_scalef32_pk_f16_fp4 v127, v120, 1.0 op_sel:[1,0,0]
	v_cvt_scalef32_pk_f16_fp4 v128, v120, 1.0 op_sel:[0,1,0]
	v_cvt_scalef32_pk_f16_fp4 v129, v120, 1.0 op_sel:[1,1,0]
	v_mfma_f32_16x16x32_f16 v[58:61], v[86:89], v[122:125], v[58:61]
	v_cvt_scalef32_pk_f16_fp4 v122, v121, 1.0
	v_cvt_scalef32_pk_f16_fp4 v123, v121, 1.0 op_sel:[1,0,0]
	v_cvt_scalef32_pk_f16_fp4 v124, v121, 1.0 op_sel:[0,1,0]
	v_cvt_scalef32_pk_f16_fp4 v125, v121, 1.0 op_sel:[1,1,0]
	v_mfma_f32_16x16x32_f16 v[62:65], v[86:89], v[126:129], v[62:65]
	v_cvt_scalef32_pk_f16_fp4 v126, v119, 1.0
	v_cvt_scalef32_pk_f16_fp4 v127, v119, 1.0 op_sel:[1,0,0]
	v_cvt_scalef32_pk_f16_fp4 v128, v119, 1.0 op_sel:[0,1,0]
	v_cvt_scalef32_pk_f16_fp4 v129, v119, 1.0 op_sel:[1,1,0]
	v_mfma_f32_16x16x32_f16 v[58:61], v[94:97], v[122:125], v[58:61]
	v_mfma_f32_16x16x32_f16 v[62:65], v[94:97], v[126:129], v[62:65]
	s_nop 7
	s_nop 7
	v_cmp_ne_u32_e32 vcc, 0, v196
	v_cndmask_b32_e32 v146, v2, v6, vcc
	v_cndmask_b32_e32 v142, v10, v14, vcc
	v_cndmask_b32_e32 v147, v18, v22, vcc
	v_cndmask_b32_e32 v143, v26, v30, vcc
	v_cndmask_b32_e32 v148, v34, v38, vcc
	v_cndmask_b32_e32 v144, v42, v46, vcc
	v_cndmask_b32_e32 v149, v50, v54, vcc
	v_cndmask_b32_e32 v145, v58, v62, vcc
	v_cmp_ne_u32_e32 vcc, 0, v197
	v_cndmask_b32_e32 v146, v146, v142, vcc
	v_cndmask_b32_e32 v147, v147, v143, vcc
	v_cndmask_b32_e32 v148, v148, v144, vcc
	v_cndmask_b32_e32 v149, v149, v145, vcc
	v_fma_f32 v142, v134, v146, v130
	v_fma_f32 v143, v135, v147, v131
	v_fma_f32 v144, v136, v148, v132
	v_fma_f32 v145, v137, v149, v133
	global_store_dword v[180:181], v142, off
	global_store_dword v[180:181], v143, off offset:256
	global_store_dword v[180:181], v144, off offset:512
	global_store_dword v[180:181], v145, off offset:768
	v_lshl_add_u64 v[180:181], v[180:181], 0, s[48:49]
	s_add_i32 s33, s33, 2
	s_cmp_lt_u32 s33, 8
	s_cbranch_scc1 .Le2_loop
	s_cmp_lt_i32 s35, 0
	s_cbranch_scc1 .Le2_exit
	s_add_i32 s39, s39, s43
	s_add_i32 s39, s39, 7
	v_mov_b32_e32 v180, v182
	v_mov_b32_e32 v181, v183
	v_mov_b32_e32 v134, v138
	v_mov_b32_e32 v135, v139
	v_mov_b32_e32 v136, v140
	v_mov_b32_e32 v137, v141
	s_mov_b32 s33, 0
	s_branch .Le2_loop
.Le2_exit:
	s_waitcnt vmcnt(0) lgkmcnt(0)
	s_branch .LBB0_878
.LBB0_899:
	s_mov_b64 s[0:1], -1
	v_writelane_b32 v255, s0, 31
	s_andn2_b64 vcc, exec, s[30:31]
	s_movk_i32 s58, 0x2c00
	v_writelane_b32 v255, s1, 32
	s_mov_b64 s[0:1], -1
	v_readlane_b32 s60, v255, 45
	v_readlane_b32 s61, v255, 46
	s_cbranch_vccz .LBB0_900
	s_getpc_b64 s[98:99]
